# attention phase: one static s_setprio 1 for waves 0-3 (the other half than before) for the whole phase, on the nt-loads stack
# speedup vs baseline: 1.0041x; 1.0041x over previous
.LBB0_2089:
	s_or_b64 exec, exec, s[8:9]
	s_waitcnt lgkmcnt(0)
	s_barrier
	s_load_dwordx2 s[0:1], s[90:91], 0xc8
	s_waitcnt vmcnt(1)
	v_lshrrev_b32_e32 v2, 1, v0
	v_and_b32_e32 v2, 6, v2
	v_and_b32_e32 v1, 3, v0
	v_lshlrev_b32_e32 v3, 3, v0
	s_waitcnt lgkmcnt(0)
	s_add_u32 s40, s0, 0x2ec00000
	s_addc_u32 s41, s1, 0
	s_add_u32 s42, s0, 0x36c00000
	s_addc_u32 s43, s1, 0
	s_add_u32 s44, s0, 0x3ec00000
	s_addc_u32 s45, s1, 0
	s_add_u32 s46, s0, 0x4fc00000
	s_addc_u32 s47, s1, 0
	s_add_u32 s48, s0, 0x1800000
	s_addc_u32 s49, s1, 0
	s_lshr_b32 s3, s57, 29
	s_add_i32 s3, s97, s3
	s_ashr_i32 s3, s3, 3
	s_mul_i32 s50, s3, s64
	v_readlane_b32 s3, v254, 12
	s_add_i32 s50, s50, s3
	v_add_u32_e32 v2, s50, v2
	v_and_b32_e32 v2, 7, v2
	v_mul_u32_u24_e32 v5, 3, v2
	v_add3_u32 v5, v5, v1, 4
	v_cmp_eq_u32_e32 vcc, 0, v1
	s_ashr_i32 s51, s50, 3
	v_and_b32_e32 v3, 0x60, v3
	v_lshl_or_b32 v4, v2, 2, v1
	v_cndmask_b32_e32 v1, v5, v2, vcc
	v_cmp_gt_u32_e32 vcc, 5, v2
	v_add_u32_e32 v3, s51, v3
	s_movk_i32 s22, 0xe000
	v_cndmask_b32_e32 v1, v4, v1, vcc
	v_lshl_add_u32 v2, v3, 5, v1
	v_ashrrev_i32_e32 v3, 31, v2
	v_lshl_add_u64 v[2:3], v[2:3], 2, s[0:1]
	s_mov_b32 s0, 0x420000
	v_add_co_u32_e32 v2, vcc, s0, v2
	s_mov_b32 s13, 0
	s_nop 0
	v_addc_co_u32_e32 v3, vcc, 0, v3, vcc
	global_load_dword v1, v[2:3], off
	v_mov_b32_e32 v3, 0
	s_mov_b64 s[14:15], 0x2000
	s_mov_b64 s[16:17], 0x4000
	s_add_i32 s69, 0, 0x14800
	s_movk_i32 s72, 0xc0
	s_mov_b64 s[18:19], 0x6000
	s_mov_b64 s[20:21], 0xa000
	s_add_i32 s73, 0, 0x14900
	s_mov_b32 s23, -1
	s_mov_b64 s[24:25], 0x8000
	s_mov_b32 s74, 0x42700000
	v_mov_b32_e32 v194, 0xff800000
	s_mov_b32 s75, 0
	v_readfirstlane_b32 s3, v0
	s_nop 3
	s_lshr_b32 s3, s3, 8
	s_cmp_lg_u32 s3, 0
	s_cbranch_scc1 .Lattn_prio_done
	s_setprio 1
